# v25 + diff-attention loops: K-fragment LDS reads issued at the loop top ahead of the DMA issue and cursor bookkeeping
# speedup vs baseline: 1.0104x; 1.0009x over previous
.LBB0_840:
	s_mul_i32 s0, s74, 0x4400
	v_add_u32_e32 v5, s0, v207
	ds_read_b128 v[6:9], v5 offset:4608
	ds_read_b128 v[10:13], v5
	ds_read_b128 v[14:17], v5 offset:32
	ds_read_b128 v[146:149], v5 offset:4640
	s_mul_i32 s2, s91, 0x4400
	s_add_i32 s3, s2, s81
	s_add_i32 s4, s2, s33
	s_and_b64 s[0:1], s[96:97], exec
	s_cselect_b32 s0, s4, s71
	s_add_i32 s1, s2, s70
	s_mov_b32 m0, s3
	s_nop 0
	global_load_lds_dwordx4 v1, s[92:93]
	s_mov_b32 m0, s0
	s_or_b64 exec, s[96:97], 1
	global_load_lds_dwordx4 v198, s[92:93]
	s_mov_b64 exec, -1
	s_mov_b32 m0, s1
	s_nop 0
	global_load_lds_dwordx4 v199, s[76:77]
	s_mov_b64 s[0:1], 0
	s_andn2_b64 vcc, exec, s[72:73]
	s_cbranch_vccnz .LBB0_851
	s_add_i32 s69, s69, -1
	s_cmp_lg_u32 s69, 0
	s_cbranch_scc0 .Ldiff_f_adv
	s_add_u32 s92, s92, 0x40000
	s_addc_u32 s93, s93, 0
	s_add_u32 s76, s76, 0x40000
	s_addc_u32 s77, s77, 0
	s_branch .LBB0_851

.LBB0_851:
	s_mul_i32 s2, s74, 0x4400
	s_add_i32 s6, s2, 0
	s_cmp_lg_u32 s10, 0
	s_cselect_b64 s[2:3], -1, 0
	s_waitcnt lgkmcnt(2)
	v_mfma_f32_32x32x16_bf16 v[130:145], v[10:13], v[178:181], v[98:113]
	s_and_b64 vcc, exec, s[2:3]
	v_mfma_f32_32x32x16_bf16 v[114:129], v[6:9], v[178:181], v[98:113]
	s_waitcnt lgkmcnt(1)
	v_mfma_f32_32x32x16_bf16 v[130:145], v[14:17], v[182:185], v[130:145]
	s_waitcnt lgkmcnt(0)
	v_mfma_f32_32x32x16_bf16 v[114:129], v[146:149], v[182:185], v[114:129]
	s_nop 9
	v_max3_f32 v2, v130, v131, v132
	v_max3_f32 v8, v133, v134, v135
	v_max3_f32 v6, v114, v115, v116
	v_max3_f32 v7, v117, v118, v119
	v_max3_f32 v2, v2, v136, v137
	v_max3_f32 v8, v8, v138, v139
	v_max3_f32 v6, v6, v120, v121
	v_max3_f32 v7, v7, v122, v123
	v_max3_f32 v2, v2, v140, v141
	v_max3_f32 v8, v8, v142, v143
	v_max3_f32 v6, v6, v124, v125
	v_max3_f32 v7, v7, v126, v127
	v_max3_f32 v2, v2, v8, v144
	v_max3_f32 v6, v6, v7, v128
	v_max_f32_e32 v7, v145, v129
	v_max3_f32 v2, v2, v6, v7
	v_mov_b32_e32 v6, v2
	s_waitcnt lgkmcnt(0)
	s_nop 1
	v_permlane32_swap_b32_e32 v6, v2
	v_max_f32_e32 v6, v2, v6
	s_cbranch_vccz .Ldf0_first
	v_cmp_lt_f32_e32 vcc, s11, v6
	s_cbranch_vccz .LBB0_858
	v_max_f32_e32 v2, v6, v6
	v_max_f32_e32 v2, 0, v2
	s_branch .Ldf0_resc

.LBB0_871:
	s_mul_i32 s0, s74, 0x4400
	v_add_u32_e32 v164, s0, v207
	ds_read_b128 v[4:7], v164 offset:4608
	ds_read_b128 v[8:11], v164
	ds_read_b128 v[12:15], v164 offset:32
	ds_read_b128 v[146:149], v164 offset:4640
	s_mul_i32 s0, s91, 0x4400
	s_add_i32 s2, s0, 0
	s_add_i32 s3, s2, s81
	s_add_i32 s4, s2, s33
	s_and_b64 s[0:1], s[96:97], exec
	s_cselect_b32 s0, s4, s71
	s_add_i32 s1, s2, s70
	s_mov_b32 s2, m0
	s_mov_b32 m0, s3
	s_nop 0
	global_load_lds_dwordx4 v1, s[92:93]
	s_mov_b32 m0, s0
	s_or_b64 exec, s[96:97], 1
	global_load_lds_dwordx4 v198, s[92:93]
	s_mov_b64 exec, -1
	s_mov_b32 m0, s1
	s_nop 0
	global_load_lds_dwordx4 v199, s[76:77]
	s_mov_b32 m0, s2
	s_andn2_b64 vcc, exec, s[72:73]
	s_mov_b64 s[0:1], 0
	s_cbranch_vccnz .LBB0_879
	s_add_i32 s69, s69, -1
	s_mov_b64 s[72:73], -1
	s_cmp_lg_u32 s69, 0
	s_mov_b64 s[6:7], -1
	s_cbranch_scc0 .LBB0_874
	s_add_u32 s2, s92, 0x40000
	s_addc_u32 s3, s93, 0
	s_add_u32 s4, s76, 0x40000
	s_addc_u32 s5, s77, 0
	s_mov_b64 s[6:7], 0

.LBB0_883:
	s_mul_i32 s2, s74, 0x4400
	s_add_i32 s83, s2, 0
	s_cmp_lg_u32 s82, -1
	s_cselect_b64 s[88:89], -1, 0
	v_sub_u32_e32 v2, v177, v176
	v_cmp_gt_i32_e64 s[2:3], v2, 59
	v_cmp_lt_i32_e64 s[6:7], v2, 59
	v_cmp_gt_i32_e64 s[24:25], v2, 18
	s_waitcnt lgkmcnt(2)
	v_mfma_f32_32x32x16_bf16 v[130:145], v[8:11], v[178:181], v[98:113]
	v_cmp_gt_i32_e64 s[26:27], v2, 49
	v_mfma_f32_32x32x16_bf16 v[114:129], v[4:7], v[178:181], v[98:113]
	v_cmp_gt_i32_e64 s[28:29], v2, 17
	v_cmp_gt_i32_e64 s[30:31], v2, 48
	v_cmp_gt_i32_e64 s[34:35], v2, 16
	v_cmp_gt_i32_e64 s[36:37], v2, 43
	v_cmp_gt_i32_e64 s[38:39], v2, 11
	v_cmp_gt_i32_e64 s[40:41], v2, 42
	v_cmp_gt_i32_e64 s[42:43], v2, 10
	s_waitcnt lgkmcnt(1)
	v_mfma_f32_32x32x16_bf16 v[130:145], v[12:15], v[182:185], v[130:145]
	v_cmp_gt_i32_e64 s[44:45], v2, 41
	v_cmp_gt_i32_e64 s[46:47], v2, 9
	v_cmp_gt_i32_e64 s[48:49], v2, 40
	v_cmp_gt_i32_e64 s[50:51], v2, 8
	s_waitcnt lgkmcnt(0)
	v_mfma_f32_32x32x16_bf16 v[114:129], v[146:149], v[182:185], v[114:129]
	v_cmp_gt_i32_e64 s[52:53], v2, 35
	v_cmp_gt_i32_e64 s[54:55], v2, 3
	v_cmp_gt_i32_e64 s[56:57], v2, 34
	v_cmp_gt_i32_e64 s[58:59], v2, 2
	v_cmp_gt_i32_e64 s[8:9], v2, 26
	v_cmp_gt_i32_e64 s[10:11], v2, 57
	v_cmp_gt_i32_e64 s[12:13], v2, 25
	v_cmp_gt_i32_e64 s[14:15], v2, 56
	v_cmp_gt_i32_e64 s[16:17], v2, 24
	v_cmp_gt_i32_e64 s[18:19], v2, 51
	v_cmp_gt_i32_e64 s[20:21], v2, 19
	v_cmp_gt_i32_e64 s[22:23], v2, 50
	v_cmp_gt_i32_e64 s[4:5], v2, 27
	v_cndmask_b32_e64 v4, v130, v243, s[2:3]
	v_cmp_gt_i32_e64 s[60:61], v2, 33
	v_cndmask_b32_e64 v160, v114, v243, s[4:5]
	v_cndmask_b32_e64 v162, v4, v130, s[6:7]
	v_cndmask_b32_e64 v163, v243, v131, s[6:7]
	v_cndmask_b32_e64 v161, v115, v243, s[8:9]
	v_cndmask_b32_e64 v156, v132, v243, s[10:11]
	v_cndmask_b32_e64 v158, v116, v243, s[12:13]
	v_cmp_gt_i32_e64 s[62:63], v2, 1
	v_cndmask_b32_e64 v157, v133, v243, s[14:15]
	v_cndmask_b32_e64 v159, v117, v243, s[16:17]
	v_cndmask_b32_e64 v152, v134, v243, s[18:19]
	v_cndmask_b32_e64 v154, v118, v243, s[20:21]
	v_cmp_gt_i32_e64 s[64:65], v2, 32
	v_max3_f32 v2, v162, v163, v156
	v_max3_f32 v114, v160, v161, v158
	v_cndmask_b32_e64 v153, v135, v243, s[22:23]
	v_cndmask_b32_e64 v155, v119, v243, s[24:25]
	v_cndmask_b32_e64 v148, v136, v243, s[26:27]
	v_cndmask_b32_e64 v150, v120, v243, s[28:29]
	v_max3_f32 v2, v2, v157, v152
	v_max3_f32 v114, v114, v159, v154
	v_cndmask_b32_e64 v149, v137, v243, s[30:31]
	v_cndmask_b32_e64 v151, v121, v243, s[34:35]
	v_cndmask_b32_e64 v10, v138, v243, s[36:37]
	v_cndmask_b32_e64 v146, v122, v243, s[38:39]
	v_max3_f32 v2, v2, v153, v148
	v_max3_f32 v114, v114, v155, v150
	v_cndmask_b32_e64 v11, v139, v243, s[40:41]
	v_cndmask_b32_e64 v147, v123, v243, s[42:43]
	v_cndmask_b32_e64 v8, v140, v243, s[44:45]
	v_cndmask_b32_e64 v12, v124, v243, s[46:47]
	v_cmp_gt_i32_e64 s[66:67], v177, v176
	v_max3_f32 v2, v2, v149, v10
	v_max3_f32 v114, v114, v151, v146
	v_cndmask_b32_e64 v9, v141, v243, s[48:49]
	v_cndmask_b32_e64 v13, v125, v243, s[50:51]
	v_cndmask_b32_e64 v4, v142, v243, s[52:53]
	v_cndmask_b32_e64 v14, v126, v243, s[54:55]
	v_cndmask_b32_e64 v7, v145, v243, s[64:65]
	v_cndmask_b32_e64 v17, v129, v243, s[66:67]
	v_max3_f32 v2, v2, v11, v8
	v_max3_f32 v114, v114, v147, v12
	v_cndmask_b32_e64 v5, v143, v243, s[56:57]
	v_cndmask_b32_e64 v15, v127, v243, s[58:59]
	v_cndmask_b32_e64 v6, v144, v243, s[60:61]
	v_cndmask_b32_e64 v16, v128, v243, s[62:63]
	v_max3_f32 v2, v2, v9, v4
	v_max3_f32 v114, v114, v13, v14
	v_max3_f32 v2, v2, v5, v6
	v_max3_f32 v114, v114, v15, v16
	v_max_f32_e32 v115, v7, v17
	v_max3_f32 v2, v2, v114, v115
	v_mov_b32_e32 v114, v2
	s_and_b64 vcc, exec, s[88:89]
	s_waitcnt lgkmcnt(0)
	s_nop 1
	v_permlane32_swap_b32_e32 v114, v2
	v_max_f32_e32 v114, v2, v114
	s_cbranch_vccz .Ldm0_first
	v_cmp_lt_f32_e32 vcc, s94, v114
	s_mov_b64 s[94:95], s[84:85]
	s_cbranch_vccz .LBB0_890
	v_max_f32_e32 v2, v114, v114
	v_max_f32_e32 v2, 0, v2
	s_branch .Ldm0_resc
